# speedup vs baseline: 1.0349x; 1.0066x over previous
_Z12fused_kernel6Params:
	s_load_dwordx16 s[52:67], s[0:1], 0x0
	s_load_dwordx16 s[36:51], s[0:1], 0x40
	s_load_dwordx16 s[8:23], s[0:1], 0x80
	s_load_dwordx4 s[24:27], s[0:1], 0xc0
	s_and_b32 s3, s2, 0x7f
	s_cmpk_gt_u32 s2, 0x7f
	v_and_b32_e32 v80, 63, v0
	s_mov_b64 s[0:1], -1
	s_mul_i32 s33, s3, 0x1c20
	s_cbranch_scc0 .Lk_217
	s_sleep 48
	v_readfirstlane_b32 s4, v0
	s_cmpk_lt_u32 s4, 0x300
	s_cbranch_scc1 .Lk_3
	s_setprio 1

.Lcb_o2r_4:
	ds_read_b128 v[56:59], v75 offset:6144
	ds_read_b128 v[60:63], v75 offset:7168
	ds_read_b128 v[44:47], v75 offset:2048
	ds_read_b128 v[68:71], v75 offset:3072
	s_cmp_eq_u32 s34, 2
	s_cbranch_scc0 .Lcb_o2s_5
	s_waitcnt lgkmcnt(4)
	v_add_f32_e32 v125, v125, v126
	v_mul_f32_e32 v126, 0x3fb8aa3b, v125
	v_exp_f32_e32 v126, v126
	v_cmp_lt_f32_e32 vcc, 0, v125
	v_mul_f32_e32 v125, 0x3f867d5f, v125
	v_fma_f32 v126, v126, v72, v73
	s_nop 0
	v_cndmask_b32_e32 v125, v126, v125, vcc
	s_mov_b64 s[16:17], exec
	s_mov_b64 exec, s[30:31]
	global_store_dword v124, v125, s[26:27] offset:0
	s_mov_b64 exec, s[16:17]
.Lcb_o2s_5:
	s_waitcnt lgkmcnt(3)
	v_mfma_f32_16x16x32_f16 v[84:87], v[30:33], v[56:59], v[84:87]
	v_mfma_f32_16x16x32_f16 v[88:91], v[22:25], v[56:59], v[88:91]
	s_waitcnt lgkmcnt(2)
	v_mfma_f32_16x16x32_f16 v[84:87], v[34:37], v[60:63], v[84:87]
	v_mfma_f32_16x16x32_f16 v[88:91], v[26:29], v[60:63], v[88:91]
	s_cmp_eq_u32 s34, 0
	s_cbranch_scc0 .Lcb_o1_6
	v_mfma_f32_16x16x32_f16 v[50:53], v[116:119], v[56:59], 0
	s_branch .Lcb_o1s_7
.Lcb_o1_6:
	s_cmp_eq_u32 s34, 1
	s_cbranch_scc0 .Lcb_o1s_7
	v_mfma_f32_16x16x32_f16 v[50:53], v[120:123], v[60:63], 0
.Lcb_o1s_7:
	s_nop 7
	v_exp_f32_e32 v94, v86
	v_exp_f32_e32 v95, v90
	v_exp_f32_e32 v96, v84
	v_exp_f32_e32 v97, v88
	v_exp_f32_e32 v98, v85
	v_exp_f32_e32 v99, v89
	s_cmp_lt_u32 s34, 2
	s_cbranch_scc0 .Lcb_o1h_8
	s_lshl_b32 s10, s34, 6
	s_cmp_eq_u32 s34, 0
	s_cselect_b32 s11, s28, 0
	v_add_f32_e32 v125, v50, v51
	v_add_f32_e32 v125, s11, v125
	v_add_u32_e32 v126, s10, v74
	s_mov_b64 s[16:17], exec
	s_mov_b64 exec, s[30:31]
	ds_write_b32 v126, v125 offset:0
	s_mov_b64 exec, s[16:17]

.Lcb_o2r_9:
	ds_read_b128 v[56:59], v75 offset:4096
	ds_read_b128 v[60:63], v75 offset:5120
	ds_read_b128 v[44:47], v75 offset:0
	ds_read_b128 v[68:71], v75 offset:1024
	s_cmp_eq_u32 s34, 2
	s_cbranch_scc0 .Lcb_o2s_10
	s_waitcnt lgkmcnt(4)
	v_add_f32_e32 v125, v125, v126
	v_mul_f32_e32 v126, 0x3fb8aa3b, v125
	v_exp_f32_e32 v126, v126
	v_cmp_lt_f32_e32 vcc, 0, v125
	v_mul_f32_e32 v125, 0x3f867d5f, v125
	v_fma_f32 v126, v126, v72, v73
	s_nop 0
	v_cndmask_b32_e32 v125, v126, v125, vcc
	s_mov_b64 s[16:17], exec
	s_mov_b64 exec, s[30:31]
	global_store_dword v124, v125, s[26:27] offset:4
	s_mov_b64 exec, s[16:17]

.Lcb_o2r_14:
	ds_read_b128 v[56:59], v75 offset:6144
	ds_read_b128 v[60:63], v75 offset:7168
	ds_read_b128 v[44:47], v75 offset:2048
	ds_read_b128 v[68:71], v75 offset:3072
	s_cmp_eq_u32 s34, 2
	s_cbranch_scc0 .Lcb_o2s_15
	s_waitcnt lgkmcnt(4)
	v_add_f32_e32 v125, v125, v126
	v_mul_f32_e32 v126, 0x3fb8aa3b, v125
	v_exp_f32_e32 v126, v126
	v_cmp_lt_f32_e32 vcc, 0, v125
	v_mul_f32_e32 v125, 0x3f867d5f, v125
	v_fma_f32 v126, v126, v72, v73
	s_nop 0
	v_cndmask_b32_e32 v125, v126, v125, vcc
	s_mov_b64 s[16:17], exec
	s_mov_b64 exec, s[30:31]
	global_store_dword v124, v125, s[26:27] offset:8
	s_mov_b64 exec, s[16:17]

.Lcb_o1_16:
	s_cmp_eq_u32 s34, 1
	s_cbranch_scc0 .Lcb_o1s_17
	v_mfma_f32_16x16x32_f16 v[50:53], v[120:123], v[60:63], 0
.Lcb_o1s_17:
	s_nop 7
	v_exp_f32_e32 v94, v86
	v_exp_f32_e32 v95, v90
	v_exp_f32_e32 v96, v84
	v_exp_f32_e32 v97, v88
	v_exp_f32_e32 v98, v85
	v_exp_f32_e32 v99, v89
	s_cmp_lt_u32 s34, 2
	s_cbranch_scc0 .Lcb_o1h_18
	s_lshl_b32 s10, s34, 6
	s_cmp_eq_u32 s34, 0
	s_cselect_b32 s11, s28, 0
	v_add_f32_e32 v125, v50, v51
	v_add_f32_e32 v125, s11, v125
	v_add_u32_e32 v126, s10, v74
	s_mov_b64 s[16:17], exec
	s_mov_b64 exec, s[30:31]
	ds_write_b32 v126, v125 offset:0
	s_mov_b64 exec, s[16:17]

.Lcb_o2r_19:
	ds_read_b128 v[56:59], v75 offset:4096
	ds_read_b128 v[60:63], v75 offset:5120
	ds_read_b128 v[44:47], v75 offset:0
	ds_read_b128 v[68:71], v75 offset:1024
	s_cmp_eq_u32 s34, 2
	s_cbranch_scc0 .Lcb_o2s_20
	s_waitcnt lgkmcnt(4)
	v_add_f32_e32 v125, v125, v126
	v_mul_f32_e32 v126, 0x3fb8aa3b, v125
	v_exp_f32_e32 v126, v126
	v_cmp_lt_f32_e32 vcc, 0, v125
	v_mul_f32_e32 v125, 0x3f867d5f, v125
	v_fma_f32 v126, v126, v72, v73
	s_nop 0
	v_cndmask_b32_e32 v125, v126, v125, vcc
	s_mov_b64 s[16:17], exec
	s_mov_b64 exec, s[30:31]
	global_store_dword v124, v125, s[26:27] offset:12
	s_mov_b64 exec, s[16:17]

.Lcb_o2r_24:
	ds_read_b128 v[56:59], v75 offset:6144
	ds_read_b128 v[60:63], v75 offset:7168
	s_cmp_eq_u32 s34, 2
	s_cbranch_scc0 .Lcb_o2s_25
	s_waitcnt lgkmcnt(2)
	v_add_f32_e32 v125, v125, v126
	v_mul_f32_e32 v126, 0x3fb8aa3b, v125
	v_exp_f32_e32 v126, v126
	v_cmp_lt_f32_e32 vcc, 0, v125
	v_mul_f32_e32 v125, 0x3f867d5f, v125
	v_fma_f32 v126, v126, v72, v73
	s_nop 0
	v_cndmask_b32_e32 v125, v126, v125, vcc
	s_mov_b64 s[16:17], exec
	s_mov_b64 exec, s[30:31]
	global_store_dword v124, v125, s[26:27] offset:0
	s_mov_b64 exec, s[16:17]
.Lcb_o2s_25:
	s_waitcnt lgkmcnt(0)
	s_cmp_eq_u32 s34, 0
	s_cbranch_scc0 .Lcb_o1_26
	v_mfma_f32_16x16x32_f16 v[50:53], v[116:119], v[56:59], 0
	s_nop 7
	v_add_f32_e32 v125, v50, v51
	v_add_f32_e32 v125, s28, v125
	s_mov_b64 s[16:17], exec
	s_mov_b64 exec, s[30:31]
	ds_write_b32 v74, v125 offset:0
	s_mov_b64 exec, s[16:17]
	s_branch .Lcb_o1s_28
.Lcb_o1_26:
	s_cmp_eq_u32 s34, 1
	s_cbranch_scc0 .Lcb_o1s_28
	v_mfma_f32_16x16x32_f16 v[50:53], v[120:123], v[60:63], 0
	s_nop 7
	v_add_f32_e32 v125, v50, v51
	s_mov_b64 s[16:17], exec
	s_mov_b64 exec, s[30:31]
	ds_write_b32 v74, v125 offset:64
	s_mov_b64 exec, s[16:17]
.Lcb_o1s_28:
	s_waitcnt lgkmcnt(0)
	s_barrier
	s_cmp_eq_u32 s34, 2
	s_cbranch_scc0 .Lcb_o2r_29
	ds_read_b32 v125, v74 offset:0
	ds_read_b32 v126, v74 offset:64
